# n29_ld6
# speedup vs baseline: 1.0070x; 1.0011x over previous
.Lrec_own_ok:
	s_barrier
	ds_read_b128 v[194:197], v180
	ds_read_b128 v[198:201], v181
	ds_read_b128 v[202:205], v182
	ds_read_b128 v[206:209], v183
	ds_read_b128 v[210:213], v184
	ds_read_b128 v[214:217], v185
	s_cmp_eq_u32 s59, 0
	s_cbranch_scc1 .Lrec_tail1
.Lrec_tail0:
	s_waitcnt lgkmcnt(5)
	v_mfma_f32_16x16x32_f16 v[154:157], v[82:85], v[194:197], v[154:157]
	ds_read_b128 v[218:221], v186
	s_waitcnt lgkmcnt(5)
	v_mfma_f32_16x16x32_f16 v[154:157], v[86:89], v[198:201], v[154:157]
	ds_read_b128 v[222:225], v187
	global_load_dwordx2 v[174:175], v243, s[52:53] nt
	s_waitcnt lgkmcnt(5)
	v_mfma_f32_16x16x32_f16 v[154:157], v[90:93], v[202:205], v[154:157]
	ds_read_b128 v[226:229], v188
	global_store_dword v242, v193, s[48:49] nt
	s_waitcnt lgkmcnt(5)
	v_mfma_f32_16x16x32_f16 v[154:157], v[94:97], v[206:209], v[154:157]
	ds_read_b128 v[230:233], v189
	s_mov_b64 exec, s[2:3]
	s_cmp_lg_u32 s57, 0
	s_cbranch_scc1 .Lrec_poi_sc1_0
	buffer_store_dwordx2 v[172:173], v165, s[8:11], s46 offen
	s_branch .Lrec_poi_done_0

.Lrec_poi_done_0:
	s_mov_b64 exec, -1
	s_waitcnt lgkmcnt(5)
	v_mfma_f32_16x16x32_f16 v[154:157], v[98:101], v[210:213], v[154:157]
	ds_read_b128 v[234:237], v190
	s_waitcnt lgkmcnt(5)
	v_mfma_f32_16x16x32_f16 v[154:157], v[102:105], v[214:217], v[154:157]
	ds_read_b128 v[238:241], v191
	s_xor_b32 s42, s42, 0x8000
	s_mov_b32 m0, s42
	s_and_b32 s36, s33, 7
	s_lshl_b32 s36, s36, 18
	s_add_u32 s40, s54, s36
	s_addc_u32 s41, s55, 0
	s_waitcnt lgkmcnt(5)
	v_mfma_f32_16x16x32_f16 v[154:157], v[106:109], v[218:221], v[154:157]
	s_add_i32 s58, s33, 1
	s_and_b32 s58, s58, 7
	s_lshl_b32 s58, s58, 18
	s_add_i32 s46, s33, 6
	s_and_b32 s46, s46, 7
	s_lshl_b32 s46, s46, 18
	s_waitcnt lgkmcnt(4)
	v_mfma_f32_16x16x32_f16 v[154:157], v[110:113], v[222:225], v[154:157]
	s_add_u32 s48, s48, 0x80000
	s_addc_u32 s49, s49, 0
	s_add_i32 s36, s33, 2
	s_min_u32 s36, s36, 0xff
	s_lshr_b32 s37, s36, 1
	s_lshl_b32 s37, s37, 21
	s_waitcnt lgkmcnt(3)
	v_mfma_f32_16x16x32_f16 v[154:157], v[114:117], v[226:229], v[154:157]
	s_and_b32 s36, s36, 1
	s_lshl_b32 s36, s36, 3
	s_or_b32 s37, s37, s36
	s_add_u32 s52, s50, s37
	s_addc_u32 s53, s51, 0
	s_waitcnt lgkmcnt(2)
	v_mfma_f32_16x16x32_f16 v[154:157], v[118:121], v[230:233], v[154:157]
	s_waitcnt lgkmcnt(1)
	v_mfma_f32_16x16x32_f16 v[154:157], v[122:125], v[234:237], v[154:157]
	s_waitcnt lgkmcnt(0)
	v_mfma_f32_16x16x32_f16 v[154:157], v[126:129], v[238:241], v[154:157]
	v_mfma_f32_16x16x32_f16 v[158:161], v[18:21], v[194:197], v[158:161]
	v_mfma_f32_16x16x32_f16 v[158:161], v[22:25], v[198:201], v[158:161]
	v_mfma_f32_16x16x32_f16 v[158:161], v[26:29], v[202:205], v[158:161]
	v_mfma_f32_16x16x32_f16 v[158:161], v[30:33], v[206:209], v[158:161]
	s_nop 3
	ds_write_b128 v178, v[154:157]
	v_mfma_f32_16x16x32_f16 v[158:161], v[34:37], v[210:213], v[158:161]
	v_mfma_f32_16x16x32_f16 v[158:161], v[38:41], v[214:217], v[158:161]
	v_mfma_f32_16x16x32_f16 v[158:161], v[42:45], v[218:221], v[158:161]
	v_mfma_f32_16x16x32_f16 v[158:161], v[46:49], v[222:225], v[158:161]
	s_waitcnt lgkmcnt(0)
	s_barrier
	ds_read_b128 v[194:197], v179
	v_mfma_f32_16x16x32_f16 v[158:161], v[50:53], v[226:229], v[158:161]
	v_mfma_f32_16x16x32_f16 v[158:161], v[54:57], v[230:233], v[158:161]
	v_mfma_f32_16x16x32_f16 v[158:161], v[58:61], v[234:237], v[158:161]
	v_mfma_f32_16x16x32_f16 v[158:161], v[62:65], v[238:241], v[158:161]
	s_nop 7
	v_pk_add_f32 v[198:199], v[158:159], v[250:251]
	v_pk_add_f32 v[200:201], v[160:161], v[252:253]
	s_branch .Lrec_act
.Lrec_tail1:
	s_waitcnt lgkmcnt(5)
	v_mfma_f32_16x16x32_f16 v[158:161], v[18:21], v[194:197], v[158:161]
	ds_read_b128 v[218:221], v186
	s_waitcnt lgkmcnt(5)
	v_mfma_f32_16x16x32_f16 v[158:161], v[22:25], v[198:201], v[158:161]
	ds_read_b128 v[222:225], v187
	global_load_dwordx2 v[174:175], v243, s[52:53] nt
	s_waitcnt lgkmcnt(5)
	v_mfma_f32_16x16x32_f16 v[158:161], v[26:29], v[202:205], v[158:161]
	ds_read_b128 v[226:229], v188
	global_store_dword v242, v193, s[48:49] nt
	s_waitcnt lgkmcnt(5)
	v_mfma_f32_16x16x32_f16 v[158:161], v[30:33], v[206:209], v[158:161]
	ds_read_b128 v[230:233], v189
	s_mov_b64 exec, s[2:3]
	s_cmp_lg_u32 s57, 0
	s_cbranch_scc1 .Lrec_poi_sc1_1
	buffer_store_dwordx2 v[172:173], v165, s[8:11], s46 offen
	s_branch .Lrec_poi_done_1

.Lrec_poi_done_1:
	s_mov_b64 exec, -1
	s_waitcnt lgkmcnt(5)
	v_mfma_f32_16x16x32_f16 v[158:161], v[34:37], v[210:213], v[158:161]
	ds_read_b128 v[234:237], v190
	s_waitcnt lgkmcnt(5)
	v_mfma_f32_16x16x32_f16 v[158:161], v[38:41], v[214:217], v[158:161]
	ds_read_b128 v[238:241], v191
	s_xor_b32 s42, s42, 0x8000
	s_mov_b32 m0, s42
	s_and_b32 s36, s33, 7
	s_lshl_b32 s36, s36, 18
	s_add_u32 s40, s54, s36
	s_addc_u32 s41, s55, 0
	s_waitcnt lgkmcnt(5)
	v_mfma_f32_16x16x32_f16 v[158:161], v[42:45], v[218:221], v[158:161]
	s_add_i32 s58, s33, 1
	s_and_b32 s58, s58, 7
	s_lshl_b32 s58, s58, 18
	s_add_i32 s46, s33, 6
	s_and_b32 s46, s46, 7
	s_lshl_b32 s46, s46, 18
	s_waitcnt lgkmcnt(4)
	v_mfma_f32_16x16x32_f16 v[158:161], v[46:49], v[222:225], v[158:161]
	s_add_u32 s48, s48, 0x80000
	s_addc_u32 s49, s49, 0
	s_add_i32 s36, s33, 2
	s_min_u32 s36, s36, 0xff
	s_lshr_b32 s37, s36, 1
	s_lshl_b32 s37, s37, 21
	s_waitcnt lgkmcnt(3)
	v_mfma_f32_16x16x32_f16 v[158:161], v[50:53], v[226:229], v[158:161]
	s_and_b32 s36, s36, 1
	s_lshl_b32 s36, s36, 3
	s_or_b32 s37, s37, s36
	s_add_u32 s52, s50, s37
	s_addc_u32 s53, s51, 0
	s_waitcnt lgkmcnt(2)
	v_mfma_f32_16x16x32_f16 v[158:161], v[54:57], v[230:233], v[158:161]
	s_waitcnt lgkmcnt(1)
	v_mfma_f32_16x16x32_f16 v[158:161], v[58:61], v[234:237], v[158:161]
	s_waitcnt lgkmcnt(0)
	v_mfma_f32_16x16x32_f16 v[158:161], v[62:65], v[238:241], v[158:161]
	v_mfma_f32_16x16x32_f16 v[154:157], v[82:85], v[194:197], v[154:157]
	v_mfma_f32_16x16x32_f16 v[154:157], v[86:89], v[198:201], v[154:157]
	v_mfma_f32_16x16x32_f16 v[154:157], v[90:93], v[202:205], v[154:157]
	v_mfma_f32_16x16x32_f16 v[154:157], v[94:97], v[206:209], v[154:157]
	s_nop 3
	ds_write_b128 v178, v[158:161]
	v_mfma_f32_16x16x32_f16 v[154:157], v[98:101], v[210:213], v[154:157]
	v_mfma_f32_16x16x32_f16 v[154:157], v[102:105], v[214:217], v[154:157]
	v_mfma_f32_16x16x32_f16 v[154:157], v[106:109], v[218:221], v[154:157]
	v_mfma_f32_16x16x32_f16 v[154:157], v[110:113], v[222:225], v[154:157]
	s_waitcnt lgkmcnt(0)
	s_barrier
	ds_read_b128 v[194:197], v179
	v_mfma_f32_16x16x32_f16 v[154:157], v[114:117], v[226:229], v[154:157]
	v_mfma_f32_16x16x32_f16 v[154:157], v[118:121], v[230:233], v[154:157]
	v_mfma_f32_16x16x32_f16 v[154:157], v[122:125], v[234:237], v[154:157]
	v_mfma_f32_16x16x32_f16 v[154:157], v[126:129], v[238:241], v[154:157]
	s_nop 7
	v_pk_add_f32 v[198:199], v[154:155], v[250:251]
	v_pk_add_f32 v[200:201], v[156:157], v[252:253]
